# P3 queue: odd workgroups start with a weight-conversion turn (turn counter initialised to blockIdx&1) so attention and conversion items overlap from t=0
# baseline (speedup 1.0000x reference)
.LBB0_407:
	s_add_u32 s0, s36, s6
	s_addc_u32 s1, s37, s7
	global_load_dwordx4 v[4:7], v1, s[0:1]
	global_load_dwordx4 v[8:11], v1, s[0:1] offset:16
	s_add_u32 s0, s38, s6
	s_addc_u32 s1, s39, s7
	global_load_dwordx4 v[12:15], v1, s[0:1]
	global_load_dwordx4 v[16:19], v1, s[0:1] offset:16
	s_add_u32 s0, s40, s6
	s_addc_u32 s1, s41, s7
	global_load_dwordx4 v[20:23], v1, s[0:1]
	global_load_dwordx4 v[24:27], v1, s[0:1] offset:16
	s_add_u32 s0, s42, s6
	s_addc_u32 s1, s43, s7
	global_load_dwordx4 v[28:31], v1, s[0:1]
	global_load_dwordx4 v[32:35], v1, s[0:1] offset:16
	s_add_u32 s6, s6, 32
	s_addc_u32 s7, s7, 0
	s_cmpk_eq_i32 s6, 0x100
	s_waitcnt vmcnt(7)
	v_mov_b32_e32 v36, v4
	v_mov_b32_e32 v4, v6
	s_waitcnt vmcnt(6)
	v_mov_b32_e32 v6, v8
	v_mov_b32_e32 v8, v10
	s_waitcnt vmcnt(5)
	v_mov_b32_e32 v10, v12
	v_mov_b32_e32 v12, v14
	s_waitcnt vmcnt(3)
	v_mov_b32_e32 v37, v20
	v_mov_b32_e32 v20, v5
	v_mov_b32_e32 v5, v22
	v_mov_b32_e32 v22, v7
	s_waitcnt vmcnt(2)
	v_mov_b32_e32 v7, v24
	v_mov_b32_e32 v24, v9
	v_mov_b32_e32 v9, v26
	v_mov_b32_e32 v26, v11
	s_waitcnt vmcnt(1)
	v_mov_b32_e32 v11, v28
	v_mov_b32_e32 v28, v13
	v_pk_fma_f32 v[2:3], v[36:37], v[10:11], v[2:3]
	v_mov_b32_e32 v13, v30
	v_pk_fma_f32 v[2:3], v[20:21], v[28:29], v[2:3]
	v_mov_b32_e32 v30, v15
	v_pk_fma_f32 v[2:3], v[4:5], v[12:13], v[2:3]
	v_mov_b32_e32 v14, v16
	s_waitcnt vmcnt(0)
	v_mov_b32_e32 v15, v32
	v_pk_fma_f32 v[2:3], v[22:23], v[30:31], v[2:3]
	v_mov_b32_e32 v32, v17
	v_pk_fma_f32 v[2:3], v[6:7], v[14:15], v[2:3]
	v_mov_b32_e32 v16, v18
	v_mov_b32_e32 v17, v34
	v_pk_fma_f32 v[2:3], v[24:25], v[32:33], v[2:3]
	v_mov_b32_e32 v34, v19
	v_pk_fma_f32 v[2:3], v[8:9], v[16:17], v[2:3]
	s_nop 0
	v_pk_fma_f32 v[2:3], v[26:27], v[34:35], v[2:3]
	s_cbranch_scc0 .LBB0_407
	v_mul_f32_e32 v1, 0x3fb8aa3b, v2
	v_mul_f32_e32 v2, 0x3fb8aa3b, v3
	v_exp_f32_e32 v1, v1
	v_exp_f32_e32 v2, v2
	s_add_u32 s0, s22, 0x4000000
	s_addc_u32 s1, s23, 0
	v_writelane_b32 v255, s0, 17
	v_sub_f32_e32 v1, v1, v2
	s_add_u32 s64, s20, 0x8000000
	v_add_f32_e32 v198, 0x3e4ccccd, v1
	v_writelane_b32 v255, s1, 18
	s_addc_u32 s65, s21, 0
	s_add_i32 s55, 0, 0x19000
	s_add_i32 s0, 0, 0x18c10
	s_mov_b32 s42, -2.0
	s_mov_b32 s48, 0xc1000000
	s_mov_b32 s50, 0xc1200000
	s_mov_b32 s56, 0xc1800000
	s_mov_b32 s58, 0xc1900000
	s_mov_b32 s60, 0xc1c00000
	s_mov_b32 s62, 0xc1d00000
	s_mov_b32 s68, 0xc2200000
	s_mov_b32 s70, 0xc2280000
	s_mov_b32 s72, 0xc2400000
	s_mov_b32 s74, 0xc2480000
	s_mov_b32 s76, 0xc2600000
	s_mov_b32 s78, 0xc2680000
	v_mov_b32_e32 v199, v198
	s_mov_b32 s41, 0
	s_mov_b64 s[6:7], -1
	v_mov_b32_e32 v3, 0
	s_movk_i32 s33, 0x2000
	s_movk_i32 s52, 0x4000
	s_movk_i32 s53, 0x6000
	s_mov_b32 s37, 0x8000
	s_mov_b32 s66, 0xa000
	s_mov_b32 s67, 0xc000
	s_mov_b32 s83, 0xe000
	s_mov_b32 s90, 0x10000
	s_mov_b32 s91, 0x12000
	s_mov_b32 s92, 0x14000
	s_mov_b32 s93, 0x16000
	s_movk_i32 s80, 0x1000
	s_movk_i32 s81, 0x3000
	s_movk_i32 s28, 0x5000
	s_mov_b32 s29, 0x40000
	s_mov_b32 s30, 0x41000
	v_writelane_b32 v255, s0, 19
	v_mov_b32_e32 v1, 0x260
	v_mov_b32_e32 v201, 2.0
	s_mov_b32 s43, 0xc0400000
	s_mov_b32 s49, 0xc1100000
	s_mov_b32 s51, 0xc1300000
	s_mov_b32 s57, 0xc1880000
	s_mov_b32 s59, 0xc1980000
	s_mov_b32 s61, 0xc1c80000
	s_mov_b32 s63, 0xc1d80000
	s_mov_b32 s69, 0xc2240000
	s_mov_b32 s71, 0xc22c0000
	s_mov_b32 s73, 0xc2440000
	s_mov_b32 s75, 0xc24c0000
	s_mov_b32 s77, 0xc2640000
	s_mov_b32 s79, 0xc26c0000
	s_mov_b32 s36, 0x41000000
	s_movk_i32 s4, 0x7fff
	v_mov_b32_e32 v213, s55
	v_mov_b32_e32 v214, 0x42800000
	v_mbcnt_hi_u32_b32 v212, -1, v196
	v_mov_b32_e32 v215, 0xf149f2ca
	s_mov_b64 s[84:85], -1
	s_and_b32 s5, s2, 1
	s_mov_b32 s32, 0
	s_branch .LBB0_412
